# nca kernels: late kernarg s_loads (out pointer before barrier 2 in nca1, KVo pointer in the softmax chain in nca0) hoisted to the prologue
# speedup vs baseline: 1.0061x; 1.0049x over previous
_Z5k_ncaILi0EEvPKDF16_S1_PKfS3_PDF16_S3_S3_S3_S3_Pf:
	s_lshl_b32 s3, s2, 1
	s_and_b32 s3, s3, 12
	s_lshr_b32 s4, s2, 6
	v_lshrrev_b32_e32 v1, 5, v0
	s_add_i32 s3, s3, s4
	s_lshl_b32 s4, s2, 6
	v_and_b32_e32 v62, 4, v1
	v_lshrrev_b32_e32 v1, 4, v0
	s_load_dwordx4 s[12:15], s[0:1], 0x0
	s_and_b32 s4, s4, 64
	s_and_b32 s2, s2, 56
	v_and_b32_e32 v63, 4, v1
	v_bfe_u32 v1, v0, 2, 2
	s_lshl_b32 s20, s3, 3
	s_or_b32 s21, s4, s2
	v_or3_b32 v2, v62, s20, v1
	v_and_b32_e32 v61, 3, v0
	v_lshl_or_b32 v2, v2, 7, s21
	v_or3_b32 v2, v2, v63, v61
	s_movk_i32 s4, 0x48
	v_mul_lo_u32 v54, v2, s4
	v_mov_b32_e32 v55, 0
	s_waitcnt lgkmcnt(0)
	v_lshl_add_u64 v[6:7], v[54:55], 1, s[12:13]
	v_and_b32_e32 v2, 48, v0
	v_mov_b32_e32 v3, v55
	v_lshl_add_u64 v[8:9], v[6:7], 0, v[2:3]
	global_load_dwordx4 v[2:5], v[8:9], off offset:64
	global_load_dwordx4 v[10:13], v[8:9], off
	global_load_dwordx4 v[22:25], v[6:7], off offset:128
	v_mul_u32_u24_e32 v6, 0x1c72, v0
	v_mul_u32_u24_e32 v65, 0x195, v0
	s_movk_i32 s2, 0xffee
	s_add_i32 s20, s20, -5
	s_add_i32 s21, s21, -5
	v_lshrrev_b32_e32 v64, 16, v6
	v_mul_i32_i24_sdwa v6, v65, s2 dst_sel:DWORD dst_unused:UNUSED_PAD src0_sel:WORD_1 src1_sel:DWORD
	v_add_u32_sdwa v14, s20, v65 dst_sel:DWORD dst_unused:UNUSED_PAD src0_sel:DWORD src1_sel:WORD_1
	v_add3_u32 v15, s21, v64, v6
	v_or_b32_e32 v6, v15, v14
	s_movk_i32 s5, 0x80
	v_cmp_gt_u32_e32 vcc, s5, v6
	v_mov_b64_e32 v[6:7], 0
	v_mov_b64_e32 v[8:9], 0
	s_and_saveexec_b64 s[2:3], vcc
	v_lshl_or_b32 v9, v14, 7, v15
	v_mad_i32_i24 v8, v64, -9, v0
	v_mul_lo_u32 v9, v9, s4
	v_lshl_add_u32 v8, v8, 3, v9
	v_ashrrev_i32_e32 v9, 31, v8
	s_or_b64 exec, exec, s[2:3]
	v_lshl_add_u64 v[8:9], v[8:9], 1, s[14:15]
	global_load_dwordx4 v[26:29], v[8:9], off
	v_or_b32_e32 v59, 0x200, v0
	v_mul_u32_u24_e32 v8, 0x1c72, v59
	v_lshrrev_b32_e32 v66, 16, v8
	v_mul_u32_u24_e32 v8, 0x653, v59
	v_lshrrev_b32_e32 v67, 18, v8
	v_mul_i32_i24_e32 v9, 0xffffffee, v67
	v_add_u32_e32 v8, s20, v67
	v_add3_u32 v9, s21, v66, v9
	v_or_b32_e32 v14, v9, v8
	v_cmp_gt_u32_e64 s[2:3], s5, v14
	s_and_saveexec_b64 s[4:5], s[2:3]
	v_lshl_or_b32 v7, v8, 7, v9
	s_movk_i32 s6, 0x48
	v_mad_i32_i24 v6, v66, -9, v59
	v_mul_lo_u32 v7, v7, s6
	v_lshl_add_u32 v6, v6, 3, v7
	v_ashrrev_i32_e32 v7, 31, v6
	s_or_b64 exec, exec, s[4:5]
	v_lshl_add_u64 v[6:7], v[6:7], 1, s[14:15]
	global_load_dwordx4 v[30:33], v[6:7], off
	v_or_b32_e32 v58, 0x400, v0
	v_mul_u32_u24_e32 v6, 0x1c72, v58
	v_lshrrev_b32_e32 v68, 16, v6
	v_mul_u32_u24_e32 v6, 0x653, v58
	v_lshrrev_b32_e32 v69, 18, v6
	v_mul_i32_i24_e32 v6, 0xffffffee, v69
	v_add_u32_e32 v14, s20, v69
	v_add3_u32 v15, s21, v68, v6
	v_or_b32_e32 v6, v15, v14
	s_movk_i32 s8, 0x80
	v_cmp_gt_u32_e64 s[4:5], s8, v6
	v_mov_b64_e32 v[6:7], 0
	v_mov_b64_e32 v[8:9], 0
	s_and_saveexec_b64 s[6:7], s[4:5]
	v_lshl_or_b32 v9, v14, 7, v15
	s_movk_i32 s9, 0x48
	v_mad_i32_i24 v8, v68, -9, v58
	v_mul_lo_u32 v9, v9, s9
	v_lshl_add_u32 v8, v8, 3, v9
	v_mov_b32_e32 v9, 0
	s_or_b64 exec, exec, s[6:7]
	v_lshl_add_u64 v[8:9], v[8:9], 1, s[14:15]
	global_load_dwordx4 v[34:37], v[8:9], off
	v_or_b32_e32 v70, 0x600, v0
	v_mul_u32_u24_e32 v8, 0x1c72, v70
	v_lshrrev_b32_e32 v71, 16, v8
	v_mul_u32_u24_e32 v8, 0x653, v70
	v_lshrrev_b32_e32 v72, 18, v8
	v_mul_i32_i24_e32 v9, 0xffffffee, v72
	v_add_u32_e32 v8, s20, v72
	v_add3_u32 v9, s21, v71, v9
	v_or_b32_e32 v14, v9, v8
	v_cmp_gt_u32_e64 s[8:9], s8, v14
	s_and_saveexec_b64 s[6:7], s[8:9]
	v_lshl_or_b32 v7, v8, 7, v9
	s_movk_i32 s10, 0x48
	v_mad_i32_i24 v6, v71, -9, v70
	v_mul_lo_u32 v7, v7, s10
	v_lshl_add_u32 v6, v6, 3, v7
	v_mov_b32_e32 v7, 0
	s_or_b64 exec, exec, s[6:7]
	v_lshl_add_u64 v[6:7], v[6:7], 1, s[14:15]
	global_load_dwordx4 v[42:45], v[6:7], off
	v_or_b32_e32 v73, 0x800, v0
	v_mul_u32_u24_e32 v6, 0x1c72, v73
	v_lshrrev_b32_e32 v14, 16, v6
	v_mul_u32_u24_e32 v6, 0xca5, v73
	s_load_dwordx2 s[12:13], s[0:1], 0x18
	v_lshrrev_b32_e32 v6, 19, v6
	v_mul_i32_i24_e32 v7, 0xffffffee, v6
	v_add_u32_e32 v15, s20, v6
	v_add3_u32 v16, s21, v14, v7
	v_or_b32_e32 v6, v16, v15
	s_movk_i32 s18, 0x80
	v_cmp_gt_u32_e64 s[10:11], s18, v6
	v_mov_b64_e32 v[6:7], 0
	v_mov_b64_e32 v[8:9], 0
	s_and_saveexec_b64 s[6:7], s[10:11]
	v_lshl_or_b32 v9, v15, 7, v16
	s_movk_i32 s16, 0x48
	v_mad_i32_i24 v8, v14, -9, v73
	v_mul_lo_u32 v9, v9, s16
	v_lshl_add_u32 v8, v8, 3, v9
	v_mov_b32_e32 v9, 0
	s_or_b64 exec, exec, s[6:7]
	v_lshl_add_u64 v[8:9], v[8:9], 1, s[14:15]
	global_load_dwordx4 v[46:49], v[8:9], off
	v_or_b32_e32 v74, 0xa00, v0
	v_min_u32_e32 v8, 0xb63, v74
	v_mul_u32_u24_e32 v14, 0xca5, v8
	s_load_dwordx2 s[16:17], s[0:1], 0x10
	s_load_dwordx2 s[64:65], s[0:1], 0x20
	v_mul_u32_u24_e32 v9, 0x1c72, v8
	v_lshrrev_b32_e32 v14, 19, v14
	v_lshrrev_b32_e32 v9, 16, v9
	v_mul_i32_i24_e32 v15, 0xffffffee, v14
	v_add_u32_e32 v14, s20, v14
	v_add3_u32 v15, s21, v9, v15
	v_or_b32_e32 v16, v15, v14
	v_cmp_gt_u32_e64 s[6:7], s18, v16
	s_and_saveexec_b64 s[18:19], s[6:7]
	v_lshl_or_b32 v7, v14, 7, v15
	s_movk_i32 s22, 0x48
	v_mad_i32_i24 v6, v9, -9, v8
	v_mul_lo_u32 v7, v7, s22
	v_lshl_add_u32 v6, v6, 3, v7
	v_mov_b32_e32 v7, 0
	s_or_b64 exec, exec, s[18:19]
	v_lshl_add_u64 v[6:7], v[6:7], 1, s[14:15]
	s_movk_i32 s14, 0xe39
	global_load_dwordx4 v[38:41], v[6:7], off
	v_mul_u32_u24_sdwa v6, v0, s14 dst_sel:DWORD dst_unused:UNUSED_PAD src0_sel:WORD_0 src1_sel:DWORD
	v_lshrrev_b32_e32 v60, 16, v6
	v_or_b32_e32 v14, 0x200, v0
	s_movk_i32 s14, 0xffee
	s_movk_i32 s15, 0x48
	v_mul_u32_u24_e32 v6, 0x48, v60
	v_mul_u32_u24_e32 v8, 0xe39, v14
	v_mad_i32_i24 v52, v60, s14, v0
	v_lshlrev_b32_e32 v50, 2, v6
	v_mov_b32_e32 v51, 0
	v_mul_i32_i24_sdwa v15, v8, s14 dst_sel:DWORD dst_unused:UNUSED_PAD src0_sel:WORD_1 src1_sel:DWORD
	v_mul_u32_u24_sdwa v8, v8, s15 dst_sel:DWORD dst_unused:UNUSED_PAD src0_sel:WORD_1 src1_sel:DWORD
	s_waitcnt lgkmcnt(0)
	v_lshl_add_u64 v[6:7], s[16:17], 0, v[50:51]
	v_lshlrev_b32_e32 v56, 2, v52
	v_lshlrev_b32_e32 v50, 2, v8
	v_add_lshl_u32 v14, v15, v14, 2
	v_ashrrev_i32_e32 v57, 31, v56
	v_lshl_add_u64 v[8:9], s[16:17], 0, v[50:51]
	v_ashrrev_i32_e32 v15, 31, v14
	v_lshl_add_u64 v[6:7], v[56:57], 2, v[6:7]
	v_lshl_add_u64 v[8:9], v[14:15], 2, v[8:9]
	global_load_dwordx4 v[18:21], v[6:7], off
	global_load_dwordx4 v[14:17], v[8:9], off
	v_min_u32_e32 v8, 0x50f, v58
	v_mul_u32_u24_e32 v6, 0xe39, v8
	v_mul_i32_i24_sdwa v9, v6, s14 dst_sel:DWORD dst_unused:UNUSED_PAD src0_sel:WORD_1 src1_sel:DWORD
	v_mul_u32_u24_sdwa v6, v6, s15 dst_sel:DWORD dst_unused:UNUSED_PAD src0_sel:WORD_1 src1_sel:DWORD
	v_lshlrev_b32_e32 v50, 2, v6
	v_add_lshl_u32 v8, v9, v8, 2
	v_lshl_add_u64 v[6:7], s[16:17], 0, v[50:51]
	v_ashrrev_i32_e32 v9, 31, v8
	v_min_u32_e32 v50, 0x47, v0
	v_lshl_add_u64 v[6:7], v[8:9], 2, v[6:7]
	v_lshlrev_b32_e32 v50, 2, v50
	global_load_dwordx4 v[6:9], v[6:7], off
	s_nop 0
	global_load_dword v57, v50, s[12:13]
	s_movk_i32 s12, 0x144
	v_cmp_gt_u32_e64 s[12:13], s12, v0
	s_and_saveexec_b64 s[14:15], s[12:13]
	s_cbranch_execz .LBB1_14
	v_mul_i32_i24_e32 v50, 0x1c72, v52
	v_lshrrev_b32_e32 v53, 31, v50
	v_add_u16_sdwa v50, v50, v53 dst_sel:DWORD dst_unused:UNUSED_PAD src0_sel:WORD_1 src1_sel:DWORD
	v_bfe_i32 v50, v50, 0, 16
	v_mul_i32_i24_e32 v53, -9, v50
	v_mad_u32_u24 v50, v60, 20, v50
	v_mul_i32_i24_e32 v50, 0xa0, v50
	v_add_lshl_u32 v52, v53, v52, 4
	v_add3_u32 v75, v50, 0, v52
	v_mov_b32_e32 v50, v51
	v_mov_b32_e32 v52, v51
	v_mov_b32_e32 v53, v51
	ds_write_b128 v75, v[50:53] offset:2880

.LBB1_16:
	s_or_b64 exec, exec, s[2:3]
	s_movk_i32 s2, 0x168
	s_waitcnt vmcnt(4)
	v_and_b32_e32 v39, 63, v0
	v_and_b32_e32 v40, 15, v0
	v_lshlrev_b32_e32 v26, 3, v50
	v_cmp_gt_u32_e32 vcc, s2, v0
	s_and_saveexec_b64 s[2:3], vcc
	s_movk_i32 s4, 0xa0
	v_mad_u32_u24 v27, v0, s4, 0
	v_mov_b32_e32 v28, 0x3c00
	ds_write_b16 v27, v28 offset:144
	s_or_b64 exec, exec, s[2:3]
	v_lshlrev_b32_e32 v38, 2, v50
	v_or_b32_e32 v28, s21, v63
	v_add_u32_e32 v29, v28, v38
	v_sub_u32_e32 v30, v38, v61
	s_movk_i32 s7, 0x80
	v_cmp_gt_u32_e64 s[2:3], 11, v30
	v_cmp_gt_u32_e64 s[4:5], s7, v29
	v_or_b32_e32 v29, 1, v38
	s_and_b64 s[2:3], s[2:3], s[4:5]
	v_mov_b32_e32 v111, 0xff800000
	v_add_u32_e32 v30, v28, v29
	v_sub_u32_e32 v29, v29, v61
	v_cndmask_b32_e64 v112, v111, 0, s[2:3]
	v_cmp_gt_u32_e64 s[2:3], 11, v29
	v_cmp_gt_u32_e64 s[4:5], s7, v30
	v_or_b32_e32 v29, 2, v38
	v_lshrrev_b32_e32 v110, 8, v0
	s_and_b64 s[2:3], s[2:3], s[4:5]
	v_add_u32_e32 v30, v28, v29
	v_sub_u32_e32 v29, v29, v61
	v_cndmask_b32_e64 v113, v111, 0, s[2:3]
	v_cmp_gt_u32_e64 s[2:3], 11, v29
	v_or_b32_e32 v29, 3, v38
	v_mad_u32_u24 v41, v110, 7, v62
	v_cmp_gt_u32_e64 s[4:5], s7, v30
	v_add_u32_e32 v28, v28, v29
	v_mad_u32_u24 v98, v41, 20, v63
	s_and_b64 s[2:3], s[2:3], s[4:5]
	v_cmp_gt_u32_e64 s[4:5], s7, v28
	v_add_u32_e32 v28, v98, v40
	s_movk_i32 s6, 0xa0
	v_mul_lo_u32 v28, v28, s6
	v_add_u32_e32 v99, 0, v28
	v_mul_u32_u24_e32 v27, 7, v110
	v_sub_u32_e32 v29, v29, v61
	v_lshl_add_u32 v94, v26, 1, v99
	s_waitcnt lgkmcnt(0)
	s_barrier
	v_cndmask_b32_e64 v114, v111, 0, s[2:3]
	v_cmp_gt_u32_e64 s[2:3], 11, v29
	ds_read_b128 v[26:29], v94
	s_and_b64 s[2:3], s[2:3], s[4:5]
	ds_read_b128 v[34:37], v94 offset:64
	v_cndmask_b32_e64 v115, v111, 0, s[2:3]
	v_cndmask_b32_e64 v30, v111, v112, s[44:45]
	v_cndmask_b32_e64 v33, v111, v115, s[44:45]
	v_cndmask_b32_e64 v32, v111, v114, s[44:45]
	v_cndmask_b32_e64 v31, v111, v113, s[44:45]
	v_cmp_gt_u32_e32 vcc, 16, v39
	v_add_u32_e32 v98, v98, v38
	s_waitcnt lgkmcnt(1)
	v_mfma_f32_16x16x32_f16 v[30:33], v[26:29], v[10:13], v[30:33]
	ds_read_b128 v[42:45], v99 offset:128
	ds_read_b128 v[46:49], v94 offset:3200
	v_cndmask_b32_e32 v29, 0, v25, vcc
	s_waitcnt lgkmcnt(2)
	v_mfma_f32_16x16x32_f16 v[30:33], v[34:37], v[2:5], v[30:33]
	v_cndmask_b32_e32 v28, 0, v24, vcc
	v_cndmask_b32_e32 v27, 0, v23, vcc
	v_cndmask_b32_e32 v26, 0, v22, vcc
	ds_read_b128 v[34:37], v94 offset:3264
	ds_read_b128 v[50:53], v99 offset:3328
	s_waitcnt lgkmcnt(3)
	v_mfma_f32_16x16x32_f16 v[22:25], v[42:45], v[26:29], v[30:33]
	ds_read_b128 v[42:45], v94 offset:6400
	ds_read_b128 v[62:65], v94 offset:6464
	v_or_b32_e32 v98, v98, v1
	v_cndmask_b32_e64 v30, v111, v112, s[46:47]
	v_cndmask_b32_e64 v33, v111, v115, s[46:47]
	v_cndmask_b32_e64 v32, v111, v114, s[46:47]
	v_cndmask_b32_e64 v31, v111, v113, s[46:47]
	v_mul_lo_u32 v98, v98, s6
	v_lshlrev_b32_e32 v61, 3, v61
	s_waitcnt lgkmcnt(4)
	v_mfma_f32_16x16x32_f16 v[30:33], v[46:49], v[10:13], v[30:33]
	ds_read_b128 v[46:49], v99 offset:6528
	ds_read_b128 v[66:69], v94 offset:9600
	v_add3_u32 v61, 0, v98, v61
	s_waitcnt lgkmcnt(5)
	v_mfma_f32_16x16x32_f16 v[30:33], v[34:37], v[2:5], v[30:33]
	v_cndmask_b32_e64 v34, v111, v112, s[48:49]
	v_cndmask_b32_e64 v37, v111, v115, s[48:49]
	v_cndmask_b32_e64 v36, v111, v114, s[48:49]
	v_cndmask_b32_e64 v35, v111, v113, s[48:49]
	ds_read_b128 v[70:73], v94 offset:9664
	ds_read_b128 v[74:77], v99 offset:9728
	s_waitcnt lgkmcnt(6)
	v_mfma_f32_16x16x32_f16 v[30:33], v[50:53], v[26:29], v[30:33]
	ds_read_b128 v[50:53], v94 offset:12800
	ds_read_b128 v[78:81], v94 offset:12864
	s_waitcnt lgkmcnt(7)
	v_mfma_f32_16x16x32_f16 v[34:37], v[42:45], v[10:13], v[34:37]
	ds_read_b128 v[42:45], v99 offset:12928
	ds_read_b128 v[82:85], v94 offset:16000
	s_waitcnt lgkmcnt(8)
	v_mfma_f32_16x16x32_f16 v[34:37], v[62:65], v[2:5], v[34:37]
	ds_read_b128 v[62:65], v94 offset:16064
	ds_read_b128 v[86:89], v99 offset:16128
	v_mul_u32_u24_e32 v128, 0xa0, v60
	s_waitcnt lgkmcnt(9)
	v_mfma_f32_16x16x32_f16 v[34:37], v[46:49], v[26:29], v[34:37]
	v_cndmask_b32_e64 v46, v111, v112, s[50:51]
	v_cndmask_b32_e64 v49, v111, v115, s[50:51]
	v_cndmask_b32_e64 v48, v111, v114, s[50:51]
	v_cndmask_b32_e64 v47, v111, v113, s[50:51]
	ds_read_b128 v[90:93], v94 offset:19200
	ds_read_b128 v[94:97], v94 offset:19264
	s_waitcnt lgkmcnt(10)
	v_mfma_f32_16x16x32_f16 v[46:49], v[66:69], v[10:13], v[46:49]
	ds_read_b128 v[66:69], v99 offset:19328
	ds_read_b64_tr_b16 v[100:101], v61 offset:3200
	v_lshlrev_b32_e32 v129, 1, v56
	s_waitcnt lgkmcnt(11)
	v_mfma_f32_16x16x32_f16 v[46:49], v[70:73], v[2:5], v[46:49]
	ds_read_b64_tr_b16 v[98:99], v61
	ds_read_b64_tr_b16 v[70:71], v61 offset:32
	s_waitcnt lgkmcnt(12)
	v_mfma_f32_16x16x32_f16 v[46:49], v[74:77], v[26:29], v[46:49]
	v_cndmask_b32_e64 v74, v111, v112, s[52:53]
	v_cndmask_b32_e64 v77, v111, v115, s[52:53]
	v_cndmask_b32_e64 v76, v111, v114, s[52:53]
	v_cndmask_b32_e64 v75, v111, v113, s[52:53]
	ds_read_b64_tr_b16 v[72:73], v61 offset:3232
	ds_read_b64_tr_b16 v[102:103], v61 offset:64
	s_waitcnt lgkmcnt(13)
	v_mfma_f32_16x16x32_f16 v[50:53], v[50:53], v[10:13], v[74:77]
	ds_read_b64_tr_b16 v[104:105], v61 offset:3264
	v_add3_u32 v128, 0, v128, v129
	s_movk_i32 s4, 0xe39
	ds_read_b64_tr_b16 v[74:75], v61 offset:96
	s_waitcnt lgkmcnt(14)
	v_mfma_f32_16x16x32_f16 v[50:53], v[78:81], v[2:5], v[50:53]
	ds_read_b64_tr_b16 v[76:77], v61 offset:3296
	ds_read_b64_tr_b16 v[78:79], v61 offset:128
	s_movk_i32 s5, 0xffee
	s_waitcnt lgkmcnt(14)
	v_mfma_f32_16x16x32_f16 v[42:45], v[42:45], v[26:29], v[50:53]
	ds_read_b64_tr_b16 v[80:81], v61 offset:3328
	ds_read_b64_tr_b16 v[106:107], v61 offset:6400
	v_cndmask_b32_e64 v50, v111, v112, s[54:55]
	v_cndmask_b32_e64 v53, v111, v115, s[54:55]
	v_cndmask_b32_e64 v52, v111, v114, s[54:55]
	v_cndmask_b32_e64 v51, v111, v113, s[54:55]
	s_nop 0
	v_mfma_f32_16x16x32_f16 v[50:53], v[82:85], v[10:13], v[50:53]
	ds_read_b64_tr_b16 v[108:109], v61 offset:9600
	ds_read_b64_tr_b16 v[82:83], v61 offset:6432
	s_waitcnt lgkmcnt(14)
	v_mfma_f32_16x16x32_f16 v[50:53], v[62:65], v[2:5], v[50:53]
	ds_read_b64_tr_b16 v[84:85], v61 offset:9632
	ds_read_b64_tr_b16 v[62:63], v61 offset:6464
	v_mfma_f32_16x16x32_f16 v[50:53], v[86:89], v[26:29], v[50:53]
	v_cndmask_b32_e64 v86, v111, v112, s[56:57]
	v_cndmask_b32_e64 v89, v111, v115, s[56:57]
	v_cndmask_b32_e64 v88, v111, v114, s[56:57]
	v_cndmask_b32_e64 v87, v111, v113, s[56:57]
	ds_read_b64_tr_b16 v[64:65], v61 offset:9664
	ds_read_b64_tr_b16 v[110:111], v61 offset:6496
	v_mfma_f32_16x16x32_f16 v[10:13], v[90:93], v[10:13], v[86:89]
	s_mov_b32 s2, 0xff800000
	ds_read_b64_tr_b16 v[112:113], v61 offset:9696
	s_nop 0
	ds_read_b64_tr_b16 v[86:87], v61 offset:6528
	v_mfma_f32_16x16x32_f16 v[2:5], v[94:97], v[2:5], v[10:13]
	ds_read_b64_tr_b16 v[88:89], v61 offset:9728
	s_nop 1
	v_max3_f32 v12, v22, s2, v23
	v_max3_f32 v12, v12, v24, v25
	v_max3_f32 v12, v12, v30, v31
	v_max3_f32 v12, v12, v32, v33
	v_max3_f32 v12, v12, v34, v35
	v_max3_f32 v12, v12, v36, v37
	v_max3_f32 v12, v12, v46, v47
	v_max3_f32 v12, v12, v48, v49
	v_mbcnt_lo_u32_b32 v13, -1, 0
	ds_read_b64_tr_b16 v[10:11], v61 offset:12800
	s_waitcnt lgkmcnt(14)
	v_mfma_f32_16x16x32_f16 v[2:5], v[66:69], v[26:29], v[2:5]
	v_max3_f32 v12, v12, v42, v43
	v_mbcnt_hi_u32_b32 v13, -1, v13
	v_max3_f32 v12, v12, v44, v45
	v_and_b32_e32 v27, 64, v13
	v_max3_f32 v12, v12, v50, v51
	v_xor_b32_e32 v26, 16, v13
	v_add_u32_e32 v27, 64, v27
	v_max3_f32 v12, v12, v52, v53
	v_cmp_lt_i32_e32 vcc, v26, v27
	v_max3_f32 v12, v12, v2, v3
	v_max3_f32 v12, v12, v4, v5
	v_mov_b32_e32 v26, v12
	s_movk_i32 s0, 0x510
	v_permlane16_swap_b32_e32 v12, v26
	v_cmp_gt_u32_e32 vcc, 11, v41
	v_mov_b32_e32 v41, 0xc80
	v_max_f32_e32 v12, v12, v26
	v_mov_b32_e32 v13, v12
	s_nop 1
	v_permlane32_swap_b32_e32 v12, v13
	s_waitcnt lgkmcnt(0)
	s_nop 0
	v_max_f32_e32 v26, v12, v13
	v_sub_f32_e32 v29, v34, v26
	v_exp_f32_e32 v92, v29
	v_sub_f32_e32 v29, v35, v26
	v_exp_f32_e32 v93, v29
	v_sub_f32_e32 v29, v36, v26
	v_exp_f32_e32 v36, v29
	v_sub_f32_e32 v29, v37, v26
	v_exp_f32_e32 v37, v29
	v_sub_f32_e32 v29, v46, v26
	v_exp_f32_e32 v94, v29
	v_sub_f32_e32 v29, v47, v26
	v_exp_f32_e32 v95, v29
	v_sub_f32_e32 v29, v48, v26
	v_sub_f32_e32 v13, v23, v26
	v_sub_f32_e32 v23, v25, v26
	v_sub_f32_e32 v25, v31, v26
	v_exp_f32_e32 v96, v29
	v_sub_f32_e32 v29, v49, v26
	v_sub_f32_e32 v12, v22, v26
	v_sub_f32_e32 v22, v24, v26
	v_sub_f32_e32 v24, v30, v26
	v_exp_f32_e32 v27, v25
	v_sub_f32_e32 v25, v32, v26
	v_sub_f32_e32 v28, v33, v26
	v_exp_f32_e32 v97, v29
	v_sub_f32_e32 v29, v42, v26
	v_exp_f32_e32 v12, v12
	v_exp_f32_e32 v13, v13
	v_exp_f32_e32 v22, v22
	v_exp_f32_e32 v23, v23
	v_exp_f32_e32 v24, v24
	v_exp_f32_e32 v25, v25
	v_exp_f32_e32 v28, v28
	v_exp_f32_e32 v114, v29
	v_sub_f32_e32 v29, v43, v26
	v_exp_f32_e32 v115, v29
	v_sub_f32_e32 v29, v44, v26
	v_exp_f32_e32 v116, v29
	v_sub_f32_e32 v29, v45, v26
	v_exp_f32_e32 v117, v29
	v_sub_f32_e32 v29, v50, v26
	v_exp_f32_e32 v118, v29
	v_sub_f32_e32 v29, v51, v26
	v_cvt_pk_f16_f32 v25, v25, v28
	v_cvt_pk_f16_f32 v24, v24, v27
	v_cvt_pk_f16_f32 v23, v22, v23
	v_cvt_pk_f16_f32 v22, v12, v13
	v_exp_f32_e32 v119, v29
	v_cndmask_b32_e32 v41, 0, v41, vcc
	v_mfma_f32_16x16x32_f16 v[28:31], v[98:101], v[22:25], 0
	ds_read_b64_tr_b16 v[12:13], v61 offset:16000
	ds_read_b64_tr_b16 v[32:33], v61 offset:12832
	v_sub_f32_e32 v27, v52, v26
	v_mfma_f32_16x16x32_f16 v[42:45], v[70:73], v[22:25], 0
	ds_read_b64_tr_b16 v[34:35], v61 offset:16032
	ds_read_b64_tr_b16 v[46:47], v61 offset:12864
	v_exp_f32_e32 v27, v27
	v_mfma_f32_16x16x32_f16 v[66:69], v[102:105], v[22:25], 0
	ds_read_b64_tr_b16 v[48:49], v61 offset:16064
	ds_read_b64_tr_b16 v[70:71], v61 offset:12896
	v_sub_f32_e32 v2, v2, v26
	v_mfma_f32_16x16x32_f16 v[74:77], v[74:77], v[22:25], 0
	ds_read_b64_tr_b16 v[72:73], v61 offset:16096
	ds_read_b64_tr_b16 v[90:91], v61 offset:12928
	v_cmp_gt_u32_e32 vcc, s0, v58
	v_mfma_f32_16x16x32_f16 v[22:25], v[78:81], v[22:25], 0
	v_cvt_pk_f16_f32 v78, v92, v93
	ds_read_b64_tr_b16 v[92:93], v61 offset:16128
	v_cvt_pk_f16_f32 v81, v96, v97
	v_cvt_pk_f16_f32 v80, v94, v95
	v_cvt_pk_f16_f32 v79, v36, v37
	v_add_u32_e32 v36, v61, v41
	v_sub_f32_e32 v37, v53, v26
	ds_read_b64_tr_b16 v[94:95], v61 offset:19200
	v_mfma_f32_16x16x32_f16 v[28:31], v[106:109], v[78:81], v[28:31]
	ds_read_b64_tr_b16 v[96:97], v36 offset:19200
	ds_read_b64_tr_b16 v[100:101], v36 offset:19232
	v_exp_f32_e32 v37, v37
	v_mfma_f32_16x16x32_f16 v[42:45], v[82:85], v[78:81], v[42:45]
	ds_read_b64_tr_b16 v[98:99], v61 offset:19232
	ds_read_b64_tr_b16 v[50:51], v61 offset:19264
	v_mfma_f32_16x16x32_f16 v[62:65], v[62:65], v[78:81], v[66:69]
	ds_read_b64_tr_b16 v[52:53], v36 offset:19264
	s_nop 1
	ds_read_b64_tr_b16 v[66:67], v61 offset:19296
	v_mfma_f32_16x16x32_f16 v[74:77], v[110:113], v[78:81], v[74:77]
	ds_read_b64_tr_b16 v[68:69], v36 offset:19296
	ds_read_b64_tr_b16 v[82:83], v61 offset:19328
	v_mfma_f32_16x16x32_f16 v[22:25], v[86:89], v[78:81], v[22:25]
	ds_read_b64_tr_b16 v[84:85], v36 offset:19328
	s_waitcnt vmcnt(2)
	v_cvt_pk_f16_f32 v21, v20, v21
	v_cvt_pk_f16_f32 v20, v18, v19
	v_cvt_pk_f16_f32 v17, v16, v17
	v_cvt_pk_f16_f32 v16, v14, v15
	ds_write_b64 v128, v[20:21] offset:57600
	v_mul_u32_u24_sdwa v18, v59, s4 dst_sel:DWORD dst_unused:UNUSED_PAD src0_sel:WORD_0 src1_sel:DWORD
	v_mul_i32_i24_sdwa v19, v18, s5 dst_sel:DWORD dst_unused:UNUSED_PAD src0_sel:WORD_1 src1_sel:DWORD
	v_mul_u32_u24_sdwa v14, v18, s6 dst_sel:DWORD dst_unused:UNUSED_PAD src0_sel:WORD_1 src1_sel:DWORD
	v_add_lshl_u32 v15, v19, v59, 3
	v_exp_f32_e32 v18, v2
	v_sub_f32_e32 v19, v3, v26
	v_sub_f32_e32 v2, v4, v26
	v_sub_f32_e32 v21, v5, v26
	v_cvt_pk_f16_f32 v81, v27, v37
	v_cvt_pk_f16_f32 v80, v118, v119
	v_cvt_pk_f16_f32 v79, v116, v117
	v_cvt_pk_f16_f32 v78, v114, v115
	v_add3_u32 v14, 0, v14, v15
	v_exp_f32_e32 v20, v2
	v_exp_f32_e32 v21, v21
	v_exp_f32_e32 v19, v19
	s_waitcnt lgkmcnt(14)
	v_mfma_f32_16x16x32_f16 v[10:13], v[10:13], v[78:81], v[28:31]
	ds_write_b64 v14, v[16:17] offset:57600
	v_mfma_f32_16x16x32_f16 v[14:17], v[32:35], v[78:81], v[42:45]
	v_mfma_f32_16x16x32_f16 v[28:31], v[46:49], v[78:81], v[62:65]
	s_nop 1
	v_mov_b32_e32 v44, 0
	v_cvt_pk_f16_f32 v43, v20, v21
	v_cvt_pk_f16_f32 v42, v18, v19
	s_waitcnt lgkmcnt(14)
	v_mfma_f32_16x16x32_f16 v[2:5], v[70:73], v[78:81], v[74:77]
	v_mov_b32_e32 v45, v44
	s_waitcnt lgkmcnt(12)
	v_mfma_f32_16x16x32_f16 v[32:35], v[90:93], v[78:81], v[22:25]
	s_waitcnt lgkmcnt(10)
	v_mfma_f32_16x16x32_f16 v[22:25], v[94:97], v[42:45], v[10:13]
	s_waitcnt lgkmcnt(8)
	v_mfma_f32_16x16x32_f16 v[18:21], v[98:101], v[42:45], v[14:17]
	s_waitcnt lgkmcnt(6)
	v_mfma_f32_16x16x32_f16 v[14:17], v[50:53], v[42:45], v[28:31]
	s_waitcnt lgkmcnt(4)
	v_mfma_f32_16x16x32_f16 v[10:13], v[66:69], v[42:45], v[2:5]
	s_waitcnt lgkmcnt(2)
	v_mfma_f32_16x16x32_f16 v[2:5], v[82:85], v[42:45], v[32:35]
	s_and_saveexec_b64 s[0:1], vcc
	s_cbranch_execz .LBB1_20
	v_mul_u32_u24_sdwa v27, v58, s4 dst_sel:DWORD dst_unused:UNUSED_PAD src0_sel:WORD_0 src1_sel:DWORD
	v_mul_i32_i24_sdwa v28, v27, s5 dst_sel:DWORD dst_unused:UNUSED_PAD src0_sel:WORD_1 src1_sel:DWORD
	s_waitcnt vmcnt(1)
	v_cvt_pk_f16_f32 v9, v8, v9
	v_cvt_pk_f16_f32 v8, v6, v7
	v_mul_u32_u24_sdwa v6, v27, s6 dst_sel:DWORD dst_unused:UNUSED_PAD src0_sel:WORD_1 src1_sel:DWORD
	v_add_lshl_u32 v7, v28, v58, 3
	v_add3_u32 v6, 0, v6, v7
	ds_write_b64 v6, v[8:9] offset:57600

.LBB1_22:
	s_or_b64 exec, exec, s[0:1]
	s_add_i32 s0, 0, 0x11880
	s_movk_i32 s1, 0x1600
	v_mov_b32_e32 v7, s0
	v_mad_u32_u24 v8, v6, s1, v7
	v_lshlrev_b32_e32 v9, 2, v39
	v_xor_b32_e32 v6, 4, v6
	v_add_u32_e32 v27, v8, v9
	v_mad_u32_u24 v6, v6, s1, v7
	ds_write2st64_b32 v27, v22, v23 offset1:1
	ds_write2st64_b32 v27, v24, v25 offset0:2 offset1:3
	ds_write2st64_b32 v27, v18, v19 offset0:4 offset1:5
	ds_write2st64_b32 v27, v20, v21 offset0:6 offset1:7
	ds_write2st64_b32 v27, v14, v15 offset0:8 offset1:9
	ds_write2st64_b32 v27, v16, v17 offset0:10 offset1:11
	ds_write2st64_b32 v27, v10, v11 offset0:12 offset1:13
	ds_write2st64_b32 v27, v12, v13 offset0:14 offset1:15
	ds_write2st64_b32 v27, v2, v3 offset0:16 offset1:17
	ds_write2st64_b32 v27, v4, v5 offset0:18 offset1:19
	ds_write_b32 v27, v26 offset:5120
	v_add_u32_e32 v27, v6, v9
	s_waitcnt lgkmcnt(0)
	s_barrier
	ds_read_b32 v122, v27 offset:5120
	v_lshlrev_b32_e32 v7, 2, v40
	v_add_u32_e32 v8, v8, v7
	v_add_u32_e32 v6, v6, v7
	ds_read_b32 v121, v6 offset:4224
	ds_read_b32 v120, v8 offset:4224
	ds_read2st64_b32 v[32:33], v27 offset0:18 offset1:19
	ds_read2st64_b32 v[34:35], v27 offset0:16 offset1:17
	ds_read2st64_b32 v[6:7], v27 offset1:1
	ds_read2st64_b32 v[8:9], v27 offset0:2 offset1:3
	ds_read2st64_b32 v[42:43], v27 offset0:4 offset1:5
	ds_read2st64_b32 v[44:45], v27 offset0:6 offset1:7
	ds_read2st64_b32 v[46:47], v27 offset0:8 offset1:9
	ds_read2st64_b32 v[48:49], v27 offset0:10 offset1:11
	ds_read2st64_b32 v[50:51], v27 offset0:12 offset1:13
	ds_read2st64_b32 v[52:53], v27 offset0:14 offset1:15
	s_waitcnt lgkmcnt(12)
	v_max_f32_e32 v123, v122, v122
	v_max_f32_e32 v28, v26, v26
	v_max_f32_e32 v28, v28, v123
	v_sub_f32_e32 v124, v26, v28
	v_sub_f32_e32 v125, v122, v28
	v_exp_f32_e32 v124, v124
	v_exp_f32_e32 v125, v125
	s_movk_i32 s0, 0x100
	s_add_i32 s1, 0, 0x10e00
	v_lshl_add_u32 v26, v38, 2, s1
	s_waitcnt lgkmcnt(10)
	v_pk_mul_f32 v[120:121], v[120:121], v[124:125]
	v_cmp_gt_u32_e64 s[0:1], s0, v0
	v_add_f32_e32 v126, v120, v121
	v_rcp_f32_e32 v126, v126
	v_cndmask_b32_e64 v56, 48, 0, s[0:1]
	v_lshl_add_u32 v41, v56, 2, v26
	ds_read_b128 v[28:31], v41
	v_mul_f32_e32 v36, v124, v126
	v_mul_f32_e32 v40, v125, v126
	s_waitcnt lgkmcnt(8)
	v_pk_mul_f32 v[6:7], v[40:41], v[6:7] op_sel_hi:[0,1]
	s_waitcnt lgkmcnt(7)
	v_pk_mul_f32 v[8:9], v[40:41], v[8:9] op_sel_hi:[0,1]
	v_pk_fma_f32 v[6:7], v[36:37], v[22:23], v[6:7] op_sel_hi:[0,1,1]
	v_pk_fma_f32 v[8:9], v[36:37], v[24:25], v[8:9] op_sel_hi:[0,1,1]
	v_cvt_pk_f16_f32 v6, v6, v7
	v_cvt_pk_f16_f32 v7, v8, v9
	s_waitcnt lgkmcnt(6)
	v_pk_mul_f32 v[8:9], v[40:41], v[42:43] op_sel_hi:[0,1]
	v_pk_fma_f32 v[8:9], v[36:37], v[18:19], v[8:9] op_sel_hi:[0,1,1]
	s_waitcnt lgkmcnt(5)
	v_pk_mul_f32 v[18:19], v[40:41], v[44:45] op_sel_hi:[0,1]
	v_pk_fma_f32 v[18:19], v[36:37], v[20:21], v[18:19] op_sel_hi:[0,1,1]
	v_cvt_pk_f16_f32 v8, v8, v9
	v_cvt_pk_f16_f32 v9, v18, v19
	s_waitcnt lgkmcnt(4)
	v_pk_mul_f32 v[18:19], v[40:41], v[46:47] op_sel_hi:[0,1]
	v_pk_fma_f32 v[14:15], v[36:37], v[14:15], v[18:19] op_sel_hi:[0,1,1]
	s_waitcnt lgkmcnt(3)
	v_pk_mul_f32 v[18:19], v[40:41], v[48:49] op_sel_hi:[0,1]
	v_pk_fma_f32 v[16:17], v[36:37], v[16:17], v[18:19] op_sel_hi:[0,1,1]
	v_cvt_pk_f16_f32 v14, v14, v15
	v_cvt_pk_f16_f32 v15, v16, v17
	s_waitcnt lgkmcnt(2)
	v_pk_mul_f32 v[16:17], v[40:41], v[50:51] op_sel_hi:[0,1]
	v_pk_fma_f32 v[10:11], v[36:37], v[10:11], v[16:17] op_sel_hi:[0,1,1]
	v_cvt_pk_f16_f32 v16, v10, v11
	s_waitcnt lgkmcnt(0)
	v_pk_mul_f32 v[10:11], v[40:41], v[52:53] op_sel_hi:[0,1]
	v_lshlrev_b32_e32 v0, 2, v0
	v_pk_fma_f32 v[10:11], v[36:37], v[12:13], v[10:11] op_sel_hi:[0,1,1]
	v_and_b32_e32 v20, 12, v0
	v_cvt_pk_f16_f32 v17, v10, v11
	v_pk_mul_f32 v[10:11], v[40:41], v[34:35] op_sel_hi:[0,1]
	v_or_b32_e32 v0, v56, v20
	v_pk_fma_f32 v[2:3], v[36:37], v[2:3], v[10:11] op_sel_hi:[0,1,1]
	v_lshlrev_b32_e32 v27, 1, v0
	v_or_b32_e32 v0, v1, v38
	v_cvt_pk_f16_f32 v10, v2, v3
	v_pk_mul_f32 v[2:3], v[40:41], v[32:33] op_sel_hi:[0,1]
	v_mul_u32_u24_e32 v0, 0x50, v0
	v_pk_fma_f32 v[2:3], v[36:37], v[4:5], v[2:3] op_sel_hi:[0,1,1]
	v_lshlrev_b32_e32 v21, 1, v0
	v_cvt_pk_f16_f32 v2, v2, v3
	v_cmp_gt_u32_e32 vcc, 32, v39
	v_add3_u32 v42, 0, v27, v21
	v_add_u32_e32 v22, 0, v21
	v_cndmask_b32_e32 v25, 0, v2, vcc
	v_add_u32_e32 v43, v22, v27
	ds_read_b64_tr_b16 v[2:3], v42 offset:57600
	ds_read_b64_tr_b16 v[4:5], v43 offset:60160
	v_and_or_b32 v0, v38, 4, v1
	s_movk_i32 s4, 0xa0
	v_mad_u32_u24 v0, v0, s4, 0
	v_add_u32_e32 v23, 0xe100, v0
	v_lshl_add_u64 v[18:19], v[54:55], 1, s[64:65]
	v_lshlrev_b32_e32 v32, 1, v38
	v_mov_b32_e32 v33, 0
	s_waitcnt lgkmcnt(0)
	v_mfma_f32_16x16x32_f16 v[0:3], v[2:5], v[6:9], v[28:31]
	v_lshl_add_u64 v[4:5], v[18:19], 0, v[32:33]
	v_add_u32_e32 v18, v23, v27
	v_cndmask_b32_e32 v24, 0, v10, vcc
	ds_read_b64_tr_b16 v[12:13], v43 offset:65280
	ds_read_b64_tr_b16 v[10:11], v42 offset:62720
	ds_read_b64_tr_b16 v[30:31], v18 offset:10240
	v_mov_b32_e32 v32, v33
	ds_read_b64_tr_b16 v[34:35], v42 offset:57632
	ds_read_b64_tr_b16 v[36:37], v43 offset:60192
	ds_read_b128 v[38:41], v41 offset:64
	s_waitcnt lgkmcnt(4)
	v_mfma_f32_16x16x32_f16 v[10:13], v[10:13], v[14:17], v[0:3]
	s_mov_b32 s2, 0xffff
	s_or_b64 s[4:5], s[0:1], vcc
	s_nop 0
	v_bfi_b32 v0, s2, v24, v24
	v_bfi_b32 v1, s2, v25, v25
	v_mov_b32_e32 v2, v33
	v_mov_b32_e32 v3, v33
	s_waitcnt lgkmcnt(0)
	v_mfma_f32_16x16x32_f16 v[34:37], v[34:37], v[6:9], v[38:41]
	v_mfma_f32_16x16x32_f16 v[10:13], v[30:33], v[0:3], v[10:13]
	ds_read_b64_tr_b16 v[44:45], v43 offset:65312
	ds_read_b64_tr_b16 v[42:43], v42 offset:62752
	ds_read_b64_tr_b16 v[30:31], v18 offset:10272
	v_lshlrev_b32_e32 v32, 1, v56
	v_lshl_add_u64 v[18:19], v[4:5], 0, v[32:33]
	v_mov_b32_e32 v32, v33
	s_waitcnt lgkmcnt(1)
	v_mfma_f32_16x16x32_f16 v[34:37], v[42:45], v[14:17], v[34:37]
	v_cvt_pk_f16_f32 v13, v12, v13
	v_cvt_pk_f16_f32 v12, v10, v11
	global_store_dwordx2 v[18:19], v[12:13], off
	s_waitcnt lgkmcnt(0)
	v_mfma_f32_16x16x32_f16 v[10:13], v[30:33], v[0:3], v[34:37]
	s_and_saveexec_b64 s[2:3], s[4:5]
	s_cbranch_execnz .LBB1_25
	s_or_b64 exec, exec, s[2:3]
	s_and_saveexec_b64 s[2:3], s[0:1]
	s_cbranch_execnz .LBB1_26

_Z5k_ncaILi1EEvPKDF16_S1_PKfS3_PDF16_S3_S3_S3_S3_Pf:
	s_lshl_b32 s3, s2, 1
	s_and_b32 s3, s3, 12
	s_lshr_b32 s4, s2, 6
	s_add_i32 s3, s3, s4
	v_lshrrev_b32_e32 v1, 5, v0
	s_lshl_b32 s4, s2, 6
	v_and_b32_e32 v76, 4, v1
	s_lshl_b32 s29, s3, 3
	s_load_dwordx4 s[20:23], s[0:1], 0x0
	s_and_b32 s4, s4, 64
	s_and_b32 s2, s2, 56
	v_bfe_u32 v60, v0, 2, 2
	v_or_b32_e32 v58, s29, v76
	s_or_b32 s28, s4, s2
	v_lshrrev_b32_e32 v52, 4, v0
	v_or_b32_e32 v2, v58, v60
	v_and_b32_e32 v57, 4, v52
	v_and_b32_e32 v1, 3, v0
	v_lshl_or_b32 v2, v2, 7, s28
	v_or3_b32 v56, v2, v57, v1
	s_movk_i32 s4, 0x48
	v_mul_lo_u32 v2, v56, s4
	v_mov_b32_e32 v3, 0
	s_waitcnt lgkmcnt(0)
	v_lshl_add_u64 v[6:7], v[2:3], 1, s[20:21]
	v_and_b32_e32 v2, 48, v0
	v_lshl_add_u64 v[8:9], v[6:7], 0, v[2:3]
	global_load_dwordx4 v[2:5], v[8:9], off offset:64
	global_load_dwordx4 v[10:13], v[8:9], off
	global_load_dwordx4 v[22:25], v[6:7], off offset:128
	v_mul_u32_u24_e32 v6, 0x1c72, v0
	v_mul_u32_u24_e32 v78, 0x195, v0
	s_movk_i32 s2, 0xffee
	s_add_i32 s29, s29, -5
	s_add_i32 s30, s28, -5
	v_lshrrev_b32_e32 v77, 16, v6
	v_mul_i32_i24_sdwa v6, v78, s2 dst_sel:DWORD dst_unused:UNUSED_PAD src0_sel:WORD_1 src1_sel:DWORD
	v_add_u32_sdwa v14, s29, v78 dst_sel:DWORD dst_unused:UNUSED_PAD src0_sel:DWORD src1_sel:WORD_1
	v_add3_u32 v15, s30, v77, v6
	v_or_b32_e32 v6, v15, v14
	s_movk_i32 s5, 0x80
	v_cmp_gt_u32_e32 vcc, s5, v6
	v_mov_b64_e32 v[6:7], 0
	v_mov_b64_e32 v[8:9], 0
	s_and_saveexec_b64 s[2:3], vcc
	v_lshl_or_b32 v9, v14, 7, v15
	v_mad_i32_i24 v8, v77, -9, v0
	v_mul_lo_u32 v9, v9, s4
	v_lshl_add_u32 v8, v8, 3, v9
	v_ashrrev_i32_e32 v9, 31, v8
	s_or_b64 exec, exec, s[2:3]
	v_lshl_add_u64 v[8:9], v[8:9], 1, s[22:23]
	global_load_dwordx4 v[26:29], v[8:9], off
	v_or_b32_e32 v62, 0x200, v0
	v_mul_u32_u24_e32 v8, 0x1c72, v62
	v_lshrrev_b32_e32 v79, 16, v8
	v_mul_u32_u24_e32 v8, 0x653, v62
	v_lshrrev_b32_e32 v80, 18, v8
	v_mul_i32_i24_e32 v9, 0xffffffee, v80
	v_add_u32_e32 v8, s29, v80
	v_add3_u32 v9, s30, v79, v9
	v_or_b32_e32 v14, v9, v8
	v_cmp_gt_u32_e64 s[2:3], s5, v14
	s_and_saveexec_b64 s[4:5], s[2:3]
	v_lshl_or_b32 v7, v8, 7, v9
	s_movk_i32 s6, 0x48
	v_mad_i32_i24 v6, v79, -9, v62
	v_mul_lo_u32 v7, v7, s6
	v_lshl_add_u32 v6, v6, 3, v7
	v_ashrrev_i32_e32 v7, 31, v6
	s_or_b64 exec, exec, s[4:5]
	v_lshl_add_u64 v[6:7], v[6:7], 1, s[22:23]
	global_load_dwordx4 v[30:33], v[6:7], off
	v_or_b32_e32 v61, 0x400, v0
	v_mul_u32_u24_e32 v6, 0x1c72, v61
	v_lshrrev_b32_e32 v81, 16, v6
	v_mul_u32_u24_e32 v6, 0x653, v61
	v_lshrrev_b32_e32 v82, 18, v6
	v_mul_i32_i24_e32 v6, 0xffffffee, v82
	v_add_u32_e32 v14, s29, v82
	v_add3_u32 v15, s30, v81, v6
	v_or_b32_e32 v6, v15, v14
	s_movk_i32 s8, 0x80
	v_cmp_gt_u32_e64 s[4:5], s8, v6
	v_mov_b64_e32 v[6:7], 0
	v_mov_b64_e32 v[8:9], 0
	s_and_saveexec_b64 s[6:7], s[4:5]
	v_lshl_or_b32 v9, v14, 7, v15
	s_movk_i32 s9, 0x48
	v_mad_i32_i24 v8, v81, -9, v61
	v_mul_lo_u32 v9, v9, s9
	v_lshl_add_u32 v8, v8, 3, v9
	v_mov_b32_e32 v9, 0
	s_or_b64 exec, exec, s[6:7]
	v_lshl_add_u64 v[8:9], v[8:9], 1, s[22:23]
	global_load_dwordx4 v[34:37], v[8:9], off
	v_or_b32_e32 v83, 0x600, v0
	v_mul_u32_u24_e32 v8, 0x1c72, v83
	v_lshrrev_b32_e32 v84, 16, v8
	v_mul_u32_u24_e32 v8, 0x653, v83
	v_lshrrev_b32_e32 v85, 18, v8
	v_mul_i32_i24_e32 v9, 0xffffffee, v85
	v_add_u32_e32 v8, s29, v85
	v_add3_u32 v9, s30, v84, v9
	v_or_b32_e32 v14, v9, v8
	v_cmp_gt_u32_e64 s[8:9], s8, v14
	s_and_saveexec_b64 s[6:7], s[8:9]
	v_lshl_or_b32 v7, v8, 7, v9
	s_movk_i32 s10, 0x48
	v_mad_i32_i24 v6, v84, -9, v83
	v_mul_lo_u32 v7, v7, s10
	v_lshl_add_u32 v6, v6, 3, v7
	v_mov_b32_e32 v7, 0
	s_or_b64 exec, exec, s[6:7]
	v_lshl_add_u64 v[6:7], v[6:7], 1, s[22:23]
	global_load_dwordx4 v[42:45], v[6:7], off
	v_or_b32_e32 v86, 0x800, v0
	v_mul_u32_u24_e32 v6, 0x1c72, v86
	v_lshrrev_b32_e32 v14, 16, v6
	v_mul_u32_u24_e32 v6, 0xca5, v86
	s_load_dwordx8 s[12:19], s[0:1], 0x28
	s_load_dwordx2 s[20:21], s[0:1], 0x18
	v_lshrrev_b32_e32 v6, 19, v6
	v_mul_i32_i24_e32 v7, 0xffffffee, v6
	v_add_u32_e32 v15, s29, v6
	v_add3_u32 v16, s30, v14, v7
	v_or_b32_e32 v6, v16, v15
	s_movk_i32 s26, 0x80
	v_cmp_gt_u32_e64 s[10:11], s26, v6
	v_mov_b64_e32 v[6:7], 0
	v_mov_b64_e32 v[8:9], 0
	s_and_saveexec_b64 s[6:7], s[10:11]
	v_lshl_or_b32 v9, v15, 7, v16
	s_movk_i32 s24, 0x48
	v_mad_i32_i24 v8, v14, -9, v86
	v_mul_lo_u32 v9, v9, s24
	v_lshl_add_u32 v8, v8, 3, v9
	v_mov_b32_e32 v9, 0
	s_or_b64 exec, exec, s[6:7]
	v_lshl_add_u64 v[8:9], v[8:9], 1, s[22:23]
	global_load_dwordx4 v[46:49], v[8:9], off
	v_or_b32_e32 v87, 0xa00, v0
	v_min_u32_e32 v8, 0xb63, v87
	v_mul_u32_u24_e32 v14, 0xca5, v8
	s_load_dwordx2 s[24:25], s[0:1], 0x10
	s_load_dwordx2 s[64:65], s[0:1], 0x48
	v_mul_u32_u24_e32 v9, 0x1c72, v8
	v_lshrrev_b32_e32 v14, 19, v14
	v_lshrrev_b32_e32 v9, 16, v9
	v_mul_i32_i24_e32 v15, 0xffffffee, v14
	v_add_u32_e32 v14, s29, v14
	v_add3_u32 v15, s30, v9, v15
	v_or_b32_e32 v16, v15, v14
	v_and_b32_e32 v59, 15, v0
	v_cmp_gt_u32_e64 s[6:7], s26, v16
	s_and_saveexec_b64 s[26:27], s[6:7]
	v_lshl_or_b32 v7, v14, 7, v15
	s_movk_i32 s31, 0x48
	v_mad_i32_i24 v6, v9, -9, v8
	v_mul_lo_u32 v7, v7, s31
	v_lshl_add_u32 v6, v6, 3, v7
	v_mov_b32_e32 v7, 0
	s_or_b64 exec, exec, s[26:27]
	v_lshl_add_u64 v[6:7], v[6:7], 1, s[22:23]
	s_movk_i32 s22, 0xe39
	global_load_dwordx4 v[38:41], v[6:7], off
	v_mul_u32_u24_sdwa v6, v0, s22 dst_sel:DWORD dst_unused:UNUSED_PAD src0_sel:WORD_0 src1_sel:DWORD
	v_lshrrev_b32_e32 v75, 16, v6
	v_or_b32_e32 v14, 0x200, v0
	s_movk_i32 s22, 0xffee
	s_movk_i32 s23, 0x48
	v_mul_u32_u24_e32 v6, 0x48, v75
	v_mul_u32_u24_e32 v8, 0xe39, v14
	v_mad_i32_i24 v53, v75, s22, v0
	v_lshlrev_b32_e32 v50, 2, v6
	v_mov_b32_e32 v51, 0
	v_mul_i32_i24_sdwa v15, v8, s22 dst_sel:DWORD dst_unused:UNUSED_PAD src0_sel:WORD_1 src1_sel:DWORD
	v_mul_u32_u24_sdwa v8, v8, s23 dst_sel:DWORD dst_unused:UNUSED_PAD src0_sel:WORD_1 src1_sel:DWORD
	s_waitcnt lgkmcnt(0)
	v_lshl_add_u64 v[6:7], s[24:25], 0, v[50:51]
	v_lshlrev_b32_e32 v54, 2, v53
	v_lshlrev_b32_e32 v50, 2, v8
	v_add_lshl_u32 v14, v15, v14, 2
	v_ashrrev_i32_e32 v55, 31, v54
	v_lshl_add_u64 v[8:9], s[24:25], 0, v[50:51]
	v_ashrrev_i32_e32 v15, 31, v14
	v_lshl_add_u64 v[6:7], v[54:55], 2, v[6:7]
	v_lshl_add_u64 v[8:9], v[14:15], 2, v[8:9]
	global_load_dwordx4 v[18:21], v[6:7], off
	global_load_dwordx4 v[14:17], v[8:9], off
	v_min_u32_e32 v8, 0x50f, v61
	v_mul_u32_u24_e32 v6, 0xe39, v8
	v_mul_i32_i24_sdwa v9, v6, s22 dst_sel:DWORD dst_unused:UNUSED_PAD src0_sel:WORD_1 src1_sel:DWORD
	v_mul_u32_u24_sdwa v6, v6, s23 dst_sel:DWORD dst_unused:UNUSED_PAD src0_sel:WORD_1 src1_sel:DWORD
	v_lshlrev_b32_e32 v50, 2, v6
	v_lshl_add_u64 v[6:7], s[24:25], 0, v[50:51]
	v_min_u32_e32 v50, 0x47, v0
	v_add_lshl_u32 v8, v9, v8, 2
	v_lshlrev_b32_e32 v50, 2, v50
	v_add_u32_e32 v63, -8, v59
	v_ashrrev_i32_e32 v9, 31, v8
	global_load_dword v68, v50, s[20:21]
	v_min_u32_e32 v50, 6, v59
	v_med3_i32 v64, v63, 0, 2
	v_mul_u32_u24_e32 v52, 7, v52
	v_and_b32_e32 v72, 15, v62
	v_lshl_add_u64 v[6:7], v[8:9], 2, v[6:7]
	v_lshlrev_b32_e32 v55, 2, v50
	v_lshlrev_b32_e32 v65, 2, v64
	v_add_lshl_u32 v50, v52, v50, 2
	v_lshrrev_b32_e32 v52, 4, v62
	v_add_u32_e32 v71, -8, v72
	global_load_dwordx4 v[6:9], v[6:7], off
	v_med3_i32 v67, v71, 0, 2
	global_load_dword v55, v55, s[14:15]
	s_nop 0
	global_load_dword v64, v65, s[18:19]
	global_load_dword v70, v65, s[16:17]
	v_min_u32_e32 v65, 6, v72
	v_mul_u32_u24_e32 v52, 7, v52
	v_add_lshl_u32 v52, v52, v65, 2
	global_load_dword v66, v50, s[12:13]
	global_load_dword v65, v52, s[12:13]
	v_mad_u32_u24 v50, 64, 3, v67
	v_add_u32_e32 v50, 0xffffff40, v50
	v_lshl_add_u64 v[88:89], v[50:51], 2, s[16:17]
	v_min_u32_e32 v50, 0x47f, v61
	v_lshrrev_b32_e32 v52, 4, v50
	v_and_b32_e32 v50, 15, v50
	v_add_u32_e32 v69, -8, v50
	s_movk_i32 s14, 0xff40
	v_min_u32_e32 v67, 6, v50
	v_med3_i32 v50, v69, 0, 2
	v_mul_u32_u24_e32 v52, 3, v52
	v_add3_u32 v50, v52, v50, s14
	global_load_dword v74, v[88:89], off
	v_lshlrev_b32_e32 v67, 2, v67
	v_lshl_add_u64 v[88:89], v[50:51], 2, s[16:17]
	global_load_dword v67, v67, s[12:13] offset:1764
	s_movk_i32 s12, 0x144
	global_load_dword v73, v[88:89], off
	v_cmp_gt_u32_e64 s[12:13], s12, v0
	s_and_saveexec_b64 s[14:15], s[12:13]
	s_cbranch_execz .LBB2_14
	v_mul_i32_i24_e32 v50, 0x1c72, v53
	v_lshrrev_b32_e32 v52, 31, v50
	v_add_u16_sdwa v50, v50, v52 dst_sel:DWORD dst_unused:UNUSED_PAD src0_sel:WORD_1 src1_sel:DWORD
	v_bfe_i32 v50, v50, 0, 16
	v_mul_i32_i24_e32 v52, -9, v50
	v_mad_u32_u24 v50, v75, 20, v50
	v_mul_i32_i24_e32 v50, 0xa0, v50
	v_add_lshl_u32 v52, v52, v53, 4
	v_add3_u32 v88, v50, 0, v52
	v_mov_b32_e32 v50, v51
	v_mov_b32_e32 v52, v51
	v_mov_b32_e32 v53, v51
	ds_write_b128 v88, v[50:53] offset:2880

.LBB2_24:
	s_or_b64 exec, exec, s[4:5]
	v_lshrrev_b32_e32 v26, 6, v0
	v_cmp_gt_u32_e32 vcc, 16, v0
	s_and_saveexec_b64 s[0:1], vcc
	s_cbranch_execz .LBB2_26
	v_cmp_gt_u32_e32 vcc, 3, v63
	s_nop 1
	v_cndmask_b32_e64 v7, 0, 1.0, vcc
	v_mul_f32_e32 v7, v7, v64
	v_fmac_f32_e32 v7, v6, v55
	v_lshl_add_u32 v6, v0, 2, 0
	v_add_u32_e32 v6, 0x11840, v6
	ds_write_b32 v6, v7
.LBB2_26:
	s_or_b64 exec, exec, s[0:1]
	s_add_i32 s0, 0, 0x11880
	s_movk_i32 s1, 0x1600
	v_mov_b32_e32 v6, s0
	v_mad_u32_u24 v7, v26, s1, v6
	v_lshlrev_b32_e32 v8, 2, v38
	v_add_u32_e32 v9, v7, v8
	ds_write2st64_b32 v9, v22, v23 offset1:1
	ds_write2st64_b32 v9, v24, v25 offset0:2 offset1:3
	ds_write2st64_b32 v9, v18, v19 offset0:4 offset1:5
	ds_write2st64_b32 v9, v20, v21 offset0:6 offset1:7
	ds_write2st64_b32 v9, v14, v15 offset0:8 offset1:9
	ds_write2st64_b32 v9, v16, v17 offset0:10 offset1:11
	ds_write2st64_b32 v9, v10, v11 offset0:12 offset1:13
	ds_write2st64_b32 v9, v12, v13 offset0:14 offset1:15
	ds_write2st64_b32 v9, v2, v3 offset0:16 offset1:17
	ds_write2st64_b32 v9, v4, v5 offset0:18 offset1:19
	ds_write_b32 v9, v28 offset:5120
	v_xor_b32_e32 v9, 4, v26
	v_mad_u32_u24 v6, v9, s1, v6
	v_add_u32_e32 v29, v6, v8
	s_waitcnt lgkmcnt(0)
	s_barrier
	ds_read_b32 v8, v29 offset:5120
	v_lshlrev_b32_e32 v27, 2, v59
	v_add_u32_e32 v7, v7, v27
	v_add_u32_e32 v6, v6, v27
	ds_read_b32 v141, v6 offset:4224
	ds_read_b32 v140, v7 offset:4224
	ds_read2st64_b32 v[36:37], v29 offset0:18 offset1:19
	ds_read2st64_b32 v[30:31], v29 offset0:16 offset1:17
	ds_read2st64_b32 v[32:33], v29 offset1:1
	ds_read2st64_b32 v[34:35], v29 offset0:2 offset1:3
	ds_read2st64_b32 v[40:41], v29 offset0:4 offset1:5
	ds_read2st64_b32 v[42:43], v29 offset0:6 offset1:7
	ds_read2st64_b32 v[48:49], v29 offset0:8 offset1:9
	ds_read2st64_b32 v[52:53], v29 offset0:10 offset1:11
	ds_read2st64_b32 v[54:55], v29 offset0:12 offset1:13
	ds_read2st64_b32 v[62:63], v29 offset0:14 offset1:15
	s_waitcnt lgkmcnt(12)
	v_max_f32_e32 v6, v8, v8
	v_max_f32_e32 v7, v28, v28
	v_max_f32_e32 v6, v7, v6
	v_sub_f32_e32 v7, v28, v6
	v_sub_f32_e32 v6, v8, v6
	v_exp_f32_e32 v142, v7
	v_exp_f32_e32 v143, v6
	v_lshl_add_u32 v28, v39, 2, 0
	v_add_u32_e32 v51, 0x10e00, v28
	ds_read_b128 v[6:9], v51
	s_waitcnt lgkmcnt(11)
	v_pk_mul_f32 v[140:141], v[140:141], v[142:143]
	s_nop 0
	v_add_f32_e32 v144, v140, v141
	v_rcp_f32_e32 v144, v144
	s_movk_i32 s0, 0xa0
	s_nop 0
	v_mul_f32_e32 v44, v142, v144
	v_mul_f32_e32 v46, v143, v144
	s_waitcnt lgkmcnt(8)
	v_pk_mul_f32 v[32:33], v[46:47], v[32:33] op_sel_hi:[0,1]
	v_pk_fma_f32 v[22:23], v[44:45], v[22:23], v[32:33] op_sel_hi:[0,1,1]
	v_cvt_pk_f16_f32 v32, v22, v23
	s_waitcnt lgkmcnt(7)
	v_pk_mul_f32 v[22:23], v[46:47], v[34:35] op_sel_hi:[0,1]
	v_pk_fma_f32 v[22:23], v[44:45], v[24:25], v[22:23] op_sel_hi:[0,1,1]
	v_cvt_pk_f16_f32 v33, v22, v23
	s_waitcnt lgkmcnt(6)
	v_pk_mul_f32 v[22:23], v[46:47], v[40:41] op_sel_hi:[0,1]
	v_pk_fma_f32 v[18:19], v[44:45], v[18:19], v[22:23] op_sel_hi:[0,1,1]
	v_cvt_pk_f16_f32 v34, v18, v19
	s_waitcnt lgkmcnt(5)
	v_pk_mul_f32 v[18:19], v[46:47], v[42:43] op_sel_hi:[0,1]
	v_pk_fma_f32 v[18:19], v[44:45], v[20:21], v[18:19] op_sel_hi:[0,1,1]
	v_cvt_pk_f16_f32 v35, v18, v19
	s_waitcnt lgkmcnt(4)
	v_pk_mul_f32 v[18:19], v[46:47], v[48:49] op_sel_hi:[0,1]
	v_pk_fma_f32 v[14:15], v[44:45], v[14:15], v[18:19] op_sel_hi:[0,1,1]
	v_cvt_pk_f16_f32 v40, v14, v15
	s_waitcnt lgkmcnt(3)
	v_pk_mul_f32 v[14:15], v[46:47], v[52:53] op_sel_hi:[0,1]
	v_pk_fma_f32 v[14:15], v[44:45], v[16:17], v[14:15] op_sel_hi:[0,1,1]
	v_cvt_pk_f16_f32 v41, v14, v15
	s_waitcnt lgkmcnt(2)
	v_pk_mul_f32 v[14:15], v[46:47], v[54:55] op_sel_hi:[0,1]
	v_pk_fma_f32 v[10:11], v[44:45], v[10:11], v[14:15] op_sel_hi:[0,1,1]
	v_cvt_pk_f16_f32 v42, v10, v11
	s_waitcnt lgkmcnt(0)
	v_pk_mul_f32 v[10:11], v[46:47], v[62:63] op_sel_hi:[0,1]
	v_pk_fma_f32 v[10:11], v[44:45], v[12:13], v[10:11] op_sel_hi:[0,1,1]
	v_cvt_pk_f16_f32 v43, v10, v11
	v_pk_mul_f32 v[10:11], v[46:47], v[30:31] op_sel_hi:[0,1]
	v_pk_fma_f32 v[2:3], v[44:45], v[2:3], v[10:11] op_sel_hi:[0,1,1]
	v_cvt_pk_f16_f32 v24, v2, v3
	v_pk_mul_f32 v[2:3], v[46:47], v[36:37] op_sel_hi:[0,1]
	v_pk_fma_f32 v[2:3], v[44:45], v[4:5], v[2:3] op_sel_hi:[0,1,1]
	v_or_b32_e32 v30, v39, v60
	v_cvt_pk_f16_f32 v2, v2, v3
	v_cmp_lt_u32_e32 vcc, 31, v38
	v_and_or_b32 v29, v39, 4, v60
	v_mul_u32_u24_e32 v3, 0x50, v30
	v_cndmask_b32_e64 v45, v2, 0, vcc
	v_mad_u32_u24 v2, v29, s0, 0
	v_lshlrev_b32_e32 v36, 3, v59
	v_lshlrev_b32_e32 v48, 1, v3
	v_add_u32_e32 v31, 0xe100, v2
	v_and_b32_e32 v2, 24, v36
	v_add_u32_e32 v49, 0, v48
	v_add_u32_e32 v44, v49, v2
	v_add_u32_e32 v37, v31, v2
	v_add3_u32 v25, 0, v2, v48
	ds_read_b64_tr_b16 v[12:13], v44 offset:60160
	ds_read_b64_tr_b16 v[10:11], v25 offset:57600
	ds_read_b64_tr_b16 v[14:15], v25 offset:62720
	ds_read_b64_tr_b16 v[16:17], v44 offset:65280
	ds_read_b64_tr_b16 v[2:3], v37 offset:10240
	ds_read_b64_tr_b16 v[18:19], v25 offset:57664
	ds_read_b64_tr_b16 v[22:23], v37 offset:10272
	ds_read_b64_tr_b16 v[54:55], v44 offset:60192
	ds_read_b64_tr_b16 v[20:21], v44 offset:60224
	ds_read_b64_tr_b16 v[62:63], v44 offset:60288
	s_waitcnt lgkmcnt(8)
	v_mfma_f32_16x16x32_f16 v[6:9], v[10:13], v[32:35], v[6:9]
	v_mov_b32_e32 v4, 0
	v_mov_b32_e32 v5, v4
	ds_read_b64_tr_b16 v[52:53], v25 offset:57632
	ds_read_b64_tr_b16 v[10:11], v25 offset:62784
	s_waitcnt vmcnt(1)
	ds_read_b64_tr_b16 v[66:67], v44 offset:65312
	ds_read_b64_tr_b16 v[12:13], v44 offset:65344
	ds_read_b64_tr_b16 v[70:71], v44 offset:65408
	s_waitcnt lgkmcnt(11)
	v_mfma_f32_16x16x32_f16 v[6:9], v[14:17], v[40:43], v[6:9]
	v_cndmask_b32_e64 v44, v24, 0, vcc
	v_mov_b32_e32 v46, v4
	v_mov_b32_e32 v47, v4
	v_mov_b32_e32 v24, v4
	v_or_b32_e32 v36, 0x60, v36
	s_waitcnt lgkmcnt(10)
	v_mfma_f32_16x16x32_f16 v[14:17], v[2:5], v[44:47], v[6:9]
	s_nop 2
	ds_read_b128 v[6:9], v51 offset:64
	s_waitcnt vmcnt(0)
	ds_read_b128 v[72:75], v51 offset:128
	ds_read_b64_tr_b16 v[2:3], v37 offset:10304
	ds_read_b64_tr_b16 v[64:65], v25 offset:62752
	ds_read_b64_tr_b16 v[68:69], v25 offset:62848
	ds_read_b64_tr_b16 v[60:61], v25 offset:57728
	v_mov_b32_e32 v25, v4
	s_waitcnt lgkmcnt(5)
	v_mfma_f32_16x16x32_f16 v[6:9], v[52:55], v[32:35], v[6:9]
	v_add3_u32 v48, 0, v36, v48
	v_add_u32_e32 v49, v49, v36
	s_movk_i32 s0, 0xff
	s_waitcnt lgkmcnt(2)
	v_mfma_f32_16x16x32_f16 v[6:9], v[64:67], v[40:43], v[6:9]
	v_cmp_lt_u32_e64 s[0:1], s0, v0
	v_mfma_f32_16x16x32_f16 v[22:25], v[22:25], v[44:47], v[6:9]
	v_mfma_f32_16x16x32_f16 v[6:9], v[18:21], v[32:35], v[72:75]
	ds_read_b64_tr_b16 v[18:19], v48 offset:57600
	ds_read_b64_tr_b16 v[20:21], v49 offset:60160
	v_mfma_f32_16x16x32_f16 v[6:9], v[10:13], v[40:43], v[6:9]
	v_mfma_f32_16x16x32_f16 v[10:13], v[2:5], v[44:47], v[6:9]
	v_add_u32_e32 v2, v31, v36
	s_nop 5
	ds_read_b128 v[6:9], v51 offset:192
	ds_read_b64_tr_b16 v[52:53], v48 offset:62720
	ds_read_b64_tr_b16 v[2:3], v2 offset:10240
	ds_read_b128 v[64:67], v51 offset:256
	ds_read_b64_tr_b16 v[54:55], v49 offset:65280
	s_waitcnt lgkmcnt(4)
	v_mfma_f32_16x16x32_f16 v[6:9], v[18:21], v[32:35], v[6:9]
	s_waitcnt lgkmcnt(0)
	v_mfma_f32_16x16x32_f16 v[6:9], v[52:55], v[40:43], v[6:9]
	v_mfma_f32_16x16x32_f16 v[18:21], v[2:5], v[44:47], v[6:9]
	ds_read_b64_tr_b16 v[2:3], v37 offset:10368
	v_mfma_f32_16x16x32_f16 v[6:9], v[60:63], v[32:35], v[64:67]
	v_mfma_f32_16x16x32_f16 v[6:9], v[68:71], v[40:43], v[6:9]
	s_waitcnt lgkmcnt(0)
	v_mfma_f32_16x16x32_f16 v[6:9], v[2:5], v[44:47], v[6:9]
	s_and_saveexec_b64 s[6:7], s[0:1]
	s_xor_b64 s[0:1], exec, s[6:7]
	s_cbranch_execz .LBB2_38
	v_lshlrev_b32_e32 v5, 2, v1
	s_add_i32 s6, 0, 0x10f40
	v_cvt_pk_f16_f32 v0, v14, v15
	v_add_u32_e32 v14, 0x11840, v28
	v_lshl_add_u32 v5, v5, 1, s6
	v_cvt_pk_f16_f32 v3, v24, v25
	v_cvt_pk_f16_f32 v2, v22, v23
	v_cvt_pk_f16_f32 v15, v20, v21
	v_lshl_add_u32 v28, v30, 5, v5
	ds_read_b128 v[20:23], v14
	ds_read_b64_tr_b16 v[24:25], v28
	ds_read_b64_tr_b16 v[26:27], v28 offset:512
	v_lshl_add_u32 v5, v29, 5, v5
	v_cvt_pk_f16_f32 v1, v16, v17
	v_cvt_pk_f16_f32 v14, v18, v19
	ds_read_b64_tr_b16 v[16:17], v28 offset:1024
	ds_read_b64_tr_b16 v[18:19], v28 offset:1536
	v_cvt_pk_f16_f32 v28, v6, v7
	ds_read_b64_tr_b16 v[6:7], v5 offset:2048
	s_waitcnt lgkmcnt(3)
	v_mfma_f32_16x16x32_f16 v[0:3], v[24:27], v[0:3], v[20:23]
	v_cvt_pk_f16_f32 v13, v12, v13
	v_cvt_pk_f16_f32 v12, v10, v11
	v_cvt_pk_f16_f32 v5, v8, v9
	v_mov_b32_e32 v8, v4
	v_mov_b32_e32 v9, v4
	s_waitcnt lgkmcnt(1)
	v_mfma_f32_16x16x32_f16 v[10:13], v[16:19], v[12:15], v[0:3]
	s_nop 2
	v_cndmask_b32_e64 v3, v5, 0, vcc
	v_cndmask_b32_e64 v2, v28, 0, vcc
	v_mov_b32_e32 v5, v4
	s_waitcnt lgkmcnt(0)
	s_nop 0
	v_mfma_f32_16x16x32_f16 v[0:3], v[6:9], v[2:5], v[10:13]
	s_and_saveexec_b64 s[6:7], s[2:3]
	s_xor_b64 s[2:3], exec, s[6:7]
	s_cbranch_execz .LBB2_35
	v_cmp_ne_u32_e32 vcc, 3, v50
	s_and_saveexec_b64 s[6:7], vcc
	s_cbranch_execz .LBB2_34
	v_cmp_ne_u32_e32 vcc, 1, v50
	s_and_saveexec_b64 s[8:9], vcc
	s_xor_b64 s[8:9], exec, s[8:9]
	v_lshl_add_u32 v4, v56, 1, v56
	v_mov_b32_e32 v5, 0
	v_lshl_add_u64 v[4:5], v[4:5], 2, s[64:65]
	s_mov_b64 s[10:11], 0x70000
	v_lshl_add_u64 v[4:5], v[4:5], 0, s[10:11]
	s_andn2_saveexec_b64 s[8:9], s[8:9]
	v_mul_lo_u32 v4, v56, 7
	v_mov_b32_e32 v5, 0
	v_lshl_add_u64 v[4:5], v[4:5], 2, s[64:65]
	v_lshl_add_u64 v[4:5], v[4:5], 0, 16
	s_or_b64 exec, exec, s[8:9]
	v_max3_f32 v3, v0, v1, v2
	v_sub_f32_e32 v0, v0, v3
	v_sub_f32_e32 v1, v1, v3
	v_mul_f32_e32 v0, 0x3fb8aa3b, v0
	v_mul_f32_e32 v1, 0x3fb8aa3b, v1
	v_sub_f32_e32 v2, v2, v3
	v_exp_f32_e32 v0, v0
	v_exp_f32_e32 v1, v1
	v_mul_f32_e32 v2, 0x3fb8aa3b, v2
	v_exp_f32_e32 v3, v2
	v_add_f32_e32 v2, v0, v1
	v_add_f32_e32 v2, v3, v2
	v_rcp_f32_e32 v2, v2
	s_nop 0
	v_pk_mul_f32 v[0:1], v[0:1], v[2:3] op_sel_hi:[1,0]
	v_mul_f32_e32 v2, v3, v2
	global_store_dwordx3 v[4:5], v[0:2], off

.LBB2_35:
	s_andn2_saveexec_b64 s[2:3], s[2:3]
	s_cbranch_execz .LBB2_37
	s_nop 2
	v_mul_f32_e32 v0, 0xbfb8aa3b, v0
	v_mul_f32_e32 v1, 0xbfb8aa3b, v1
	v_mul_f32_e32 v2, 0xbfb8aa3b, v2
	v_mul_f32_e32 v3, 0xbfb8aa3b, v3
	v_exp_f32_e32 v0, v0
	v_exp_f32_e32 v1, v1
	v_exp_f32_e32 v2, v2
	v_exp_f32_e32 v3, v3
	v_mul_lo_u32 v4, v56, 7
	v_mov_b32_e32 v5, 0
	v_pk_add_f32 v[0:1], v[0:1], 1.0 op_sel_hi:[1,0]
	v_pk_add_f32 v[2:3], v[2:3], 1.0 op_sel_hi:[1,0]
	v_lshl_add_u64 v[4:5], v[4:5], 2, s[64:65]
	v_rcp_f32_e32 v0, v0
	v_rcp_f32_e32 v1, v1
	v_rcp_f32_e32 v2, v2
	v_rcp_f32_e32 v3, v3
	s_nop 0
	global_store_dwordx4 v[4:5], v[0:3], off

.LBB2_38:
	s_andn2_saveexec_b64 s[0:1], s[0:1]
	s_cbranch_execz .LBB2_41
	v_and_b32_e32 v0, 3, v26
	v_mul_u32_u24_e32 v0, 0x1100, v0
	s_add_i32 s0, 0, 0x1c880
	v_mul_u32_u24_e32 v1, 0x110, v59
	v_add3_u32 v0, s0, v0, v1
	v_lshl_add_u32 v1, v39, 2, v0
	ds_write_b128 v1, v[14:17]
	ds_write_b128 v1, v[22:25] offset:64
	ds_write_b128 v1, v[10:13] offset:128
	ds_write_b128 v1, v[18:21] offset:192
	v_lshlrev_b32_e32 v1, 8, v59
	s_movk_i32 s2, 0x110
	v_sub_u32_e32 v4, v0, v1
	v_lshlrev_b32_e32 v0, 2, v27
	v_mov_b32_e32 v1, 0
	v_lshl_add_u64 v[2:3], s[64:65], 0, v[0:1]
	s_mov_b64 s[0:1], 0xa0000
	v_mad_u32_u24 v18, v50, s2, v4
	v_lshl_add_u64 v[14:15], v[2:3], 0, s[0:1]
	ds_read_b128 v[2:5], v18
	v_lshl_or_b32 v0, v58, 7, v57
	v_or3_b32 v0, v0, s28, v50
	ds_read_b128 v[10:13], v18 offset:1088
	v_lshlrev_b32_e32 v0, 6, v0
	v_lshl_add_u64 v[16:17], v[0:1], 2, v[14:15]
	s_waitcnt lgkmcnt(1)
	global_store_dwordx4 v[16:17], v[2:5], off nt
	v_or_b32_e32 v16, 0x4000, v0
	v_mov_b32_e32 v17, v1
	v_or_b32_e32 v2, 0x2000, v0
	v_mov_b32_e32 v3, v1
	v_lshl_add_u64 v[2:3], v[2:3], 2, v[14:15]
	s_waitcnt lgkmcnt(0)
	global_store_dwordx4 v[2:3], v[10:13], off nt
	ds_read_b128 v[2:5], v18 offset:2176
	ds_read_b128 v[10:13], v18 offset:3264
	v_lshl_add_u64 v[16:17], v[16:17], 2, v[14:15]
	v_or_b32_e32 v0, 0x6000, v0
	v_cmp_gt_u32_e32 vcc, 32, v38
	s_waitcnt lgkmcnt(1)
	global_store_dwordx4 v[16:17], v[2:5], off nt
	s_nop 1
	v_lshl_add_u64 v[2:3], v[0:1], 2, v[14:15]
	s_waitcnt lgkmcnt(0)
	global_store_dwordx4 v[2:3], v[10:13], off nt
	s_and_saveexec_b64 s[0:1], vcc
	s_cbranch_execz .LBB2_41
	v_lshlrev_b32_e32 v0, 3, v56
	v_lshl_add_u64 v[2:3], v[0:1], 2, s[64:65]
	v_lshlrev_b32_e32 v0, 2, v39
	v_lshl_add_u64 v[0:1], v[2:3], 0, v[0:1]
	v_add_co_u32_e32 v0, vcc, 0x4a0000, v0
	s_nop 1
	v_addc_co_u32_e32 v1, vcc, 0, v1, vcc
	global_store_dwordx4 v[0:1], v[6:9], off
